# dead-code removal: 8 zero-inits of registers fully rewritten by the two cvt_pk_fp8 halves in the attention-hosted MoE-down store
# speedup vs baseline: 1.0006x; 1.0006x over previous
;     __device__ __forceinline__ bool next(int i, Unit& u) const { if (!T.tile(i, u.pm, u.pn)) return false; u.aoff = (size_t)u.pm * atile; u.boff = (size_t)u.pn * btile; return true; }
;     __device__ __forceinline__ bool next(int i, Unit& u) const { if (!T.tile(i, u.pm, u.pn)) return false; u.aoff = (size_t)u.pm * 256 * D * 2 + (size_t)(u.pn >> 1) * 512; u.boff = (size_t)u.pn * 256 * 256 * 2; return true; }
;     __device__ __forceinline__ bool next(int i, Unit& u) const { if (!T.tile(i, u.pm, u.pn)) return false; const int e = tile_e[u.pm] & 7; u.aoff = (size_t)u.pm * atile; u.boff = ((size_t)e * nN + u.pn) * btile; return true; }
; __device__ __forceinline__ void cvt_store(CvtState& cs, int lane, const f32x4 (&v)[8]) {
;     const int kb = cs.next % CV_KB, tmp = cs.next / CV_KB, nb = tmp % CV_NB, e = tmp / CV_NB;
;     unsigned char* dst = cs.WT + ((size_t)e * D + (size_t)(16 * nb + 4 * (lane & 3))) * FF + 128 * kb + 8 * (lane >> 2);
; #pragma unroll
;     for (int j = 0; j < 4; ++j) { u32x2 w; w.x = pk4_fp8(v[0][j] * CV_WS, v[1][j] * CV_WS, v[2][j] * CV_WS, v[3][j] * CV_WS); w.y = pk4_fp8(v[4][j] * CV_WS, v[5][j] * CV_WS, v[6][j] * CV_WS, v[7][j] * CV_WS);
;         *(u32x2*)(dst + (size_t)j * FF) = w; }
;     ++cs.next;
.LBB0_1044:
	s_mul_hi_i32 s18, s35, 0x92492493
	s_add_i32 s18, s18, s35
	s_ashr_i32 s19, s18, 5
	s_lshr_b32 s20, s18, 31
	s_add_i32 s19, s19, s20
	s_ashr_i32 s46, s19, 31
	s_lshr_b32 s46, s46, 25
	s_add_i32 s46, s19, s46
	s_and_b32 s46, s46, 0xfffff80
	s_ashr_i32 s18, s18, 12
	s_sub_i32 s46, s19, s46
	s_add_i32 s18, s18, s20
	s_mul_i32 s21, s19, 56
	s_ashr_i32 s19, s18, 31
	v_lshl_or_b32 v74, s46, 4, v202
	s_lshl_b64 s[18:19], s[18:19], 11
	v_ashrrev_i32_e32 v75, 31, v74
	v_lshl_add_u64 v[74:75], s[18:19], 0, v[74:75]
	v_mov_b64_e32 v[76:77], s[30:31]
	v_mad_u64_u32 v[76:77], s[18:19], v74, s61, v[76:77]
	v_mad_i32_i24 v77, v75, s61, v77
	s_waitcnt vmcnt(14)
	v_mul_f32_e32 v74, 0x42800000, v158
	s_waitcnt vmcnt(13)
	v_mul_f32_e32 v75, 0x42800000, v162
	v_med3_f32 v79, v74, s53, v203
	v_med3_f32 v75, v75, s53, v203
	v_cvt_pk_fp8_f32 v74, v79, v75
	s_waitcnt vmcnt(12)
	v_mul_f32_e32 v78, 0x42800000, v166
	s_waitcnt vmcnt(11)
	v_mul_f32_e32 v75, 0x42800000, v170
	v_med3_f32 v78, v78, s53, v203
	v_med3_f32 v75, v75, s53, v203
	v_cvt_pk_fp8_f32 v74, v78, v75 op_sel:[0,0,1]
	s_waitcnt vmcnt(10)
	v_mul_f32_e32 v75, 0x42800000, v174
	s_waitcnt vmcnt(9)
	v_mul_f32_e32 v78, 0x42800000, v178
	v_med3_f32 v80, v75, s53, v203
	v_med3_f32 v78, v78, s53, v203
	v_cvt_pk_fp8_f32 v75, v80, v78
	s_waitcnt vmcnt(8)
	v_mul_f32_e32 v79, 0x42800000, v182
	s_waitcnt vmcnt(7)
	v_mul_f32_e32 v78, 0x42800000, v186
	s_sub_i32 s21, s35, s21
	v_med3_f32 v79, v79, s53, v203
	v_med3_f32 v78, v78, s53, v203
	s_lshl_b32 s18, s21, 7
	v_cvt_pk_fp8_f32 v75, v79, v78 op_sel:[0,0,1]
	s_ashr_i32 s19, s18, 31
	v_lshl_add_u64 v[76:77], v[76:77], 0, s[18:19]
	v_lshl_add_u64 v[76:77], v[76:77], 0, v[204:205]
	global_store_dwordx2 v[76:77], v[74:75], off
	v_mul_f32_e32 v74, 0x42800000, v159
	v_mul_f32_e32 v75, 0x42800000, v163
	v_med3_f32 v79, v74, s53, v203
	v_med3_f32 v75, v75, s53, v203
	v_cvt_pk_fp8_f32 v74, v79, v75
	v_mul_f32_e32 v78, 0x42800000, v167
	v_mul_f32_e32 v75, 0x42800000, v171
	v_med3_f32 v78, v78, s53, v203
	v_med3_f32 v75, v75, s53, v203
	v_cvt_pk_fp8_f32 v74, v78, v75 op_sel:[0,0,1]
	v_mul_f32_e32 v75, 0x42800000, v175
	v_mul_f32_e32 v78, 0x42800000, v179
	v_med3_f32 v80, v75, s53, v203
	v_med3_f32 v78, v78, s53, v203
	v_cvt_pk_fp8_f32 v75, v80, v78
	v_mul_f32_e32 v79, 0x42800000, v183
	v_mul_f32_e32 v78, 0x42800000, v187
	v_med3_f32 v79, v79, s53, v203
	v_med3_f32 v78, v78, s53, v203
	v_cvt_pk_fp8_f32 v75, v79, v78 op_sel:[0,0,1]
	s_movk_i32 s18, 0x1000
	v_add_co_u32_e32 v78, vcc, s18, v76
	s_add_i32 s35, s35, 1
	s_nop 0
	v_addc_co_u32_e32 v79, vcc, 0, v77, vcc
	global_store_dwordx2 v[78:79], v[74:75], off offset:3072
	v_mul_f32_e32 v74, 0x42800000, v160
	v_mul_f32_e32 v75, 0x42800000, v164
	v_med3_f32 v79, v74, s53, v203
	v_med3_f32 v75, v75, s53, v203
	v_cvt_pk_fp8_f32 v74, v79, v75
	v_mul_f32_e32 v78, 0x42800000, v168
	v_mul_f32_e32 v75, 0x42800000, v172
	v_med3_f32 v78, v78, s53, v203
	v_med3_f32 v75, v75, s53, v203
	v_cvt_pk_fp8_f32 v74, v78, v75 op_sel:[0,0,1]
	v_mul_f32_e32 v75, 0x42800000, v176
	v_mul_f32_e32 v78, 0x42800000, v180
	v_med3_f32 v80, v75, s53, v203
	v_med3_f32 v78, v78, s53, v203
	v_cvt_pk_fp8_f32 v75, v80, v78
	v_mul_f32_e32 v79, 0x42800000, v184
	v_mul_f32_e32 v78, 0x42800000, v188
	v_med3_f32 v79, v79, s53, v203
	v_med3_f32 v78, v78, s53, v203
	v_cvt_pk_fp8_f32 v75, v79, v78 op_sel:[0,0,1]
	v_add_co_u32_e32 v78, vcc, s55, v76
	s_nop 1
	v_addc_co_u32_e32 v79, vcc, 0, v77, vcc
	global_store_dwordx2 v[78:79], v[74:75], off offset:2048
	v_mul_f32_e32 v74, 0x42800000, v161
	v_mul_f32_e32 v75, 0x42800000, v165
	v_med3_f32 v79, v74, s53, v203
	v_med3_f32 v75, v75, s53, v203
	v_cvt_pk_fp8_f32 v74, v79, v75
	v_mul_f32_e32 v78, 0x42800000, v169
	v_mul_f32_e32 v75, 0x42800000, v173
	v_med3_f32 v78, v78, s53, v203
	v_med3_f32 v75, v75, s53, v203
	v_cvt_pk_fp8_f32 v74, v78, v75 op_sel:[0,0,1]
	v_mul_f32_e32 v75, 0x42800000, v177
	v_mul_f32_e32 v78, 0x42800000, v181
	v_med3_f32 v80, v75, s53, v203
	v_med3_f32 v78, v78, s53, v203
	v_cvt_pk_fp8_f32 v75, v80, v78
	v_mul_f32_e32 v79, 0x42800000, v185
	v_mul_f32_e32 v78, 0x42800000, v189
	v_med3_f32 v79, v79, s53, v203
	v_med3_f32 v78, v78, s53, v203
	v_cvt_pk_fp8_f32 v75, v79, v78 op_sel:[0,0,1]
	v_add_co_u32_e32 v76, vcc, 0x5000, v76
	s_nop 1
	v_addc_co_u32_e32 v77, vcc, 0, v77, vcc
	global_store_dwordx2 v[76:77], v[74:75], off offset:1024
	s_and_b64 s[18:19], s[38:39], s[42:43]
	s_andn2_b64 vcc, exec, s[18:19]
	s_cbranch_vccz .LBB0_1031
	s_branch .LBB0_1032
